# dilated attention band-edge masks folded into bias table (-1e30 entries), one pad s_nop; second measure
# speedup vs baseline: 1.0049x; 1.0049x over previous
.LBB0_1520:
	s_or_b64 exec, exec, s[34:35]
	s_ashr_i32 s50, s41, 6
	s_lshl_b32 s51, s82, 8
	s_lshl_b32 s46, s50, 5
	s_lshl_b32 s36, s83, 11
	s_add_i32 s46, s46, s51
	s_and_b64 s[34:35], s[4:5], exec
	s_movk_i32 s34, 0x80
	s_cselect_b32 s37, 0x200, s34
	s_and_b64 s[34:35], s[10:11], exec
	v_and_b32_e32 v138, 31, v4
	s_cselect_b32 s47, 0x800, s37
	s_and_b64 s[4:5], s[4:5], exec
	v_or_b32_e32 v136, s46, v138
	s_cselect_b32 s34, 2, 4
	s_and_b64 s[4:5], s[10:11], exec
	v_cmp_gt_i32_e32 vcc, s47, v136
	s_cselect_b32 s45, 0, s34
	s_lshl_b32 s4, s40, 23
	v_cndmask_b32_e32 v2, 0, v136, vcc
	s_add_u32 s4, s16, s4
	v_lshlrev_b32_e32 v2, s45, v2
	s_addc_u32 s5, s17, 0
	s_or_b32 s35, s36, s7
	v_add_u32_e32 v8, s35, v2
	v_ashrrev_i32_e32 v9, 31, v8
	v_lshlrev_b64 v[8:9], 9, v[8:9]
	v_bfe_u32 v6, v4, 5, 1
	v_lshl_add_u64 v[8:9], s[4:5], 0, v[8:9]
	s_lshl_b32 s48, s6, 7
	v_lshl_add_u64 v[8:9], v[8:9], 0, s[48:49]
	v_lshlrev_b32_e32 v2, 4, v6
	v_lshl_add_u64 v[8:9], v[8:9], 0, v[2:3]
	s_mov_b64 s[10:11], 0x4000000
	v_lshl_add_u64 v[132:133], v[8:9], 0, s[10:11]
	v_add_co_u32_e32 v8, vcc, 0x4000000, v8
	s_movk_i32 s10, 0x100
	s_nop 0
	v_addc_co_u32_e32 v9, vcc, 0, v9, vcc
	global_load_dwordx4 v[116:119], v[132:133], off offset:32
	global_load_dwordx4 v[120:123], v[132:133], off offset:64
	global_load_dwordx4 v[124:127], v[8:9], off
	global_load_dwordx4 v[128:131], v[132:133], off offset:96
	s_lshl_b32 s34, s40, 2
	v_cmp_gt_i32_e32 vcc, s10, v4
	s_and_saveexec_b64 s[10:11], vcc
	s_cbranch_execz .LBB0_1524
	v_cmp_lt_i32_e32 vcc, 63, v4
	v_mov_b32_e32 v2, 0xf149f2ca
	s_nop 0
	s_and_saveexec_b64 s[38:39], vcc
	s_cbranch_execz .LBB0_1523
	s_or_b32 s37, s34, s6
	s_mul_i32 s48, s37, 0xc0
	s_lshl_b64 s[40:41], s[48:49], 2
	s_add_u32 s40, s0, s40
	s_addc_u32 s41, s1, s41
	v_mov_b32_e32 v5, v3
	v_lshl_add_u64 v[8:9], v[4:5], 2, s[40:41]
	v_add_co_u32_e32 v8, vcc, 0x129000, v8
	s_nop 1
	v_addc_co_u32_e32 v9, vcc, 0, v9, vcc
	global_load_dword v2, v[8:9], off offset:768
